# attention output epilogues (MoBA partials, dilated outputs): eight 8-byte row stores per lane paired into four 16-byte stores with v_permlane32_swap (same bytes, same addresses)
# speedup vs baseline: 1.0119x; 1.0055x over previous
.LBB0_271:
	ds_bpermute_b32 v50, v161, v146
	s_ashr_i32 s15, s14, 31
	v_mov_b32_e32 v157, v1
	s_waitcnt lgkmcnt(0)
	v_add_f32_e32 v50, v146, v50
	v_div_scale_f32 v51, s[34:35], v50, v50, 1.0
	v_rcp_f32_e32 v52, v51
	s_lshl_b64 s[34:35], s[14:15], 25
	s_add_u32 s34, s11, s34
	s_addc_u32 s35, s26, s35
	v_fma_f32 v53, -v51, v52, 1.0
	v_fmac_f32_e32 v52, v53, v52
	v_div_scale_f32 v53, vcc, 1.0, v50, 1.0
	v_mul_f32_e32 v54, v53, v52
	v_fma_f32 v55, -v51, v54, v53
	v_fmac_f32_e32 v54, v55, v52
	v_fma_f32 v51, -v51, v54, v53
	v_div_fmas_f32 v51, v51, v52, v54
	v_lshlrev_b64 v[54:55], 11, v[158:159]
	v_div_fixup_f32 v52, v51, v50, 1.0
	v_lshl_add_u64 v[54:55], s[34:35], 0, v[54:55]
	s_lshl_b32 s56, s16, 1
	v_lshl_add_u64 v[54:55], v[54:55], 0, s[56:57]
	v_lshl_add_u64 v[54:55], v[54:55], 0, v[156:157]
	v_mbcnt_lo_u32_b32 v196, -1, 0
	v_and_b32_e32 v196, 32, v196
	v_lshrrev_b32_e32 v196, 2, v196
	v_mov_b32_e32 v197, 0
	s_nop 0
	v_lshl_add_u64 v[54:55], v[54:55], 0, v[196:197]
	v_pk_mul_f32 v[56:57], v[34:35], v[52:53] op_sel_hi:[1,0]
	v_pk_mul_f32 v[58:59], v[36:37], v[52:53] op_sel_hi:[1,0]
	v_pk_mul_f32 v[60:61], v[38:39], v[52:53] op_sel_hi:[1,0]
	v_pk_mul_f32 v[62:63], v[40:41], v[52:53] op_sel_hi:[1,0]
	v_cvt_pk_bf16_f32 v192, v56, v57
	v_cvt_pk_bf16_f32 v193, v58, v59
	v_cvt_pk_bf16_f32 v194, v60, v61
	v_cvt_pk_bf16_f32 v195, v62, v63
	s_nop 1
	v_permlane32_swap_b32_e32 v192, v194
	v_permlane32_swap_b32_e32 v193, v195
	global_store_dwordx4 v[54:55], v[192:195], off
	v_pk_mul_f32 v[56:57], v[42:43], v[52:53] op_sel_hi:[1,0]
	v_pk_mul_f32 v[58:59], v[44:45], v[52:53] op_sel_hi:[1,0]
	v_pk_mul_f32 v[60:61], v[46:47], v[52:53] op_sel_hi:[1,0]
	v_pk_mul_f32 v[62:63], v[48:49], v[52:53] op_sel_hi:[1,0]
	v_cvt_pk_bf16_f32 v192, v56, v57
	v_cvt_pk_bf16_f32 v193, v58, v59
	v_cvt_pk_bf16_f32 v194, v60, v61
	v_cvt_pk_bf16_f32 v195, v62, v63
	s_nop 1
	v_permlane32_swap_b32_e32 v192, v194
	v_permlane32_swap_b32_e32 v193, v195
	global_store_dwordx4 v[54:55], v[192:195], off offset:32
	v_pk_mul_f32 v[56:57], v[18:19], v[52:53] op_sel_hi:[1,0]
	v_pk_mul_f32 v[58:59], v[20:21], v[52:53] op_sel_hi:[1,0]
	v_pk_mul_f32 v[60:61], v[22:23], v[52:53] op_sel_hi:[1,0]
	v_pk_mul_f32 v[62:63], v[24:25], v[52:53] op_sel_hi:[1,0]
	v_cvt_pk_bf16_f32 v192, v56, v57
	v_cvt_pk_bf16_f32 v193, v58, v59
	v_cvt_pk_bf16_f32 v194, v60, v61
	v_cvt_pk_bf16_f32 v195, v62, v63
	s_nop 1
	v_permlane32_swap_b32_e32 v192, v194
	v_permlane32_swap_b32_e32 v193, v195
	global_store_dwordx4 v[54:55], v[192:195], off offset:64
	v_pk_mul_f32 v[56:57], v[26:27], v[52:53] op_sel_hi:[1,0]
	v_pk_mul_f32 v[58:59], v[28:29], v[52:53] op_sel_hi:[1,0]
	v_pk_mul_f32 v[60:61], v[30:31], v[52:53] op_sel_hi:[1,0]
	v_pk_mul_f32 v[62:63], v[32:33], v[52:53] op_sel_hi:[1,0]
	v_cvt_pk_bf16_f32 v192, v56, v57
	v_cvt_pk_bf16_f32 v193, v58, v59
	v_cvt_pk_bf16_f32 v194, v60, v61
	v_cvt_pk_bf16_f32 v195, v62, v63
	s_nop 1
	v_permlane32_swap_b32_e32 v192, v194
	v_permlane32_swap_b32_e32 v193, v195
	global_store_dwordx4 v[54:55], v[192:195], off offset:96
	s_and_saveexec_b64 s[16:17], s[40:41]
	s_cbranch_execz .LBB0_234
	v_cmp_gt_f32_e32 vcc, s80, v50
	s_mov_b32 s19, 0x3f317217
	s_lshl_b64 s[14:15], s[14:15], 20
	v_cndmask_b32_e64 v18, 0, 32, vcc
	v_ldexp_f32 v18, v50, v18
	v_log_f32_e32 v18, v18
	v_cndmask_b32_e32 v19, 0, v226, vcc
	s_add_u32 s14, s27, s14
	s_addc_u32 s15, s28, s15
	v_mul_f32_e32 v20, 0x3f317217, v18
	v_fma_f32 v20, v18, s19, -v20
	v_fmac_f32_e32 v20, 0x3377d1cf, v18
	s_mov_b32 s19, 0x7f800000
	v_fmac_f32_e32 v20, 0x3f317217, v18
	v_cmp_lt_f32_e64 vcc, |v18|, s19
	s_lshl_b32 s56, s31, 2
	s_nop 0
	v_cndmask_b32_e32 v18, v18, v20, vcc
	v_sub_f32_e32 v20, v18, v19
	v_lshlrev_b64 v[18:19], 6, v[158:159]
	v_lshl_add_u64 v[18:19], s[14:15], 0, v[18:19]
	v_fmac_f32_e32 v20, 0x3f317218, v189
	v_lshl_add_u64 v[18:19], v[18:19], 0, s[56:57]
	global_store_dword v[18:19], v20, off
	s_branch .LBB0_234

.LBB0_816:
	s_waitcnt lgkmcnt(2)
	ds_bpermute_b32 v2, v164, v205
	v_cmp_lt_i32_e32 vcc, v201, v155
	v_ashrrev_i32_e32 v159, 31, v158
	s_or_b64 s[18:19], s[16:17], vcc
	s_and_saveexec_b64 s[16:17], s[18:19]
	s_cbranch_execz .LBB0_783
	s_waitcnt lgkmcnt(0)
	v_add_f32_e32 v4, v205, v2
	v_div_scale_f32 v2, s[18:19], v4, v4, 1.0
	v_rcp_f32_e32 v3, v2
	v_div_scale_f32 v5, vcc, 1.0, v4, 1.0
	v_fma_f32 v6, -v2, v3, 1.0
	v_fmac_f32_e32 v3, v6, v3
	v_mul_f32_e32 v6, v5, v3
	v_fma_f32 v7, -v2, v6, v5
	v_fmac_f32_e32 v6, v7, v3
	v_fma_f32 v2, -v2, v6, v5
	v_div_fmas_f32 v2, v2, v3, v6
	v_div_fixup_f32 v6, v2, v4, 1.0
	v_lshlrev_b64 v[2:3], 6, v[158:159]
	v_or_b32_e32 v2, s27, v2
	v_lshl_add_u64 v[2:3], v[2:3], 0, v[160:161]
	v_lshlrev_b64 v[8:9], 7, v[2:3]
	v_lshl_add_u64 v[8:9], v[152:153], 0, v[8:9]
	v_mbcnt_lo_u32_b32 v44, -1, 0
	v_and_b32_e32 v44, 32, v44
	v_lshrrev_b32_e32 v44, 2, v44
	v_mov_b32_e32 v45, 0
	s_nop 0
	v_lshl_add_u64 v[8:9], v[8:9], 0, v[44:45]
	v_pk_mul_f32 v[32:33], v[48:49], v[6:7] op_sel_hi:[1,0]
	v_pk_mul_f32 v[34:35], v[50:51], v[6:7] op_sel_hi:[1,0]
	v_pk_mul_f32 v[36:37], v[52:53], v[6:7] op_sel_hi:[1,0]
	v_pk_mul_f32 v[38:39], v[54:55], v[6:7] op_sel_hi:[1,0]
	v_cvt_pk_bf16_f32 v40, v32, v33
	v_cvt_pk_bf16_f32 v41, v34, v35
	v_cvt_pk_bf16_f32 v42, v36, v37
	v_cvt_pk_bf16_f32 v43, v38, v39
	s_nop 1
	v_permlane32_swap_b32_e32 v40, v42
	v_permlane32_swap_b32_e32 v41, v43
	global_store_dwordx4 v[8:9], v[40:43], off
	v_pk_mul_f32 v[32:33], v[56:57], v[6:7] op_sel_hi:[1,0]
	v_pk_mul_f32 v[34:35], v[58:59], v[6:7] op_sel_hi:[1,0]
	v_pk_mul_f32 v[36:37], v[60:61], v[6:7] op_sel_hi:[1,0]
	v_pk_mul_f32 v[38:39], v[62:63], v[6:7] op_sel_hi:[1,0]
	v_cvt_pk_bf16_f32 v40, v32, v33
	v_cvt_pk_bf16_f32 v41, v34, v35
	v_cvt_pk_bf16_f32 v42, v36, v37
	v_cvt_pk_bf16_f32 v43, v38, v39
	s_nop 1
	v_permlane32_swap_b32_e32 v40, v42
	v_permlane32_swap_b32_e32 v41, v43
	global_store_dwordx4 v[8:9], v[40:43], off offset:32
	v_pk_mul_f32 v[32:33], v[64:65], v[6:7] op_sel_hi:[1,0]
	v_pk_mul_f32 v[34:35], v[66:67], v[6:7] op_sel_hi:[1,0]
	v_pk_mul_f32 v[36:37], v[68:69], v[6:7] op_sel_hi:[1,0]
	v_pk_mul_f32 v[38:39], v[70:71], v[6:7] op_sel_hi:[1,0]
	v_cvt_pk_bf16_f32 v40, v32, v33
	v_cvt_pk_bf16_f32 v41, v34, v35
	v_cvt_pk_bf16_f32 v42, v36, v37
	v_cvt_pk_bf16_f32 v43, v38, v39
	s_nop 1
	v_permlane32_swap_b32_e32 v40, v42
	v_permlane32_swap_b32_e32 v41, v43
	global_store_dwordx4 v[8:9], v[40:43], off offset:64
	v_pk_mul_f32 v[32:33], v[72:73], v[6:7] op_sel_hi:[1,0]
	v_pk_mul_f32 v[34:35], v[74:75], v[6:7] op_sel_hi:[1,0]
	v_pk_mul_f32 v[36:37], v[76:77], v[6:7] op_sel_hi:[1,0]
	v_pk_mul_f32 v[38:39], v[78:79], v[6:7] op_sel_hi:[1,0]
	v_cvt_pk_bf16_f32 v40, v32, v33
	v_cvt_pk_bf16_f32 v41, v34, v35
	v_cvt_pk_bf16_f32 v42, v36, v37
	v_cvt_pk_bf16_f32 v43, v38, v39
	s_nop 1
	v_permlane32_swap_b32_e32 v40, v42
	v_permlane32_swap_b32_e32 v41, v43
	global_store_dwordx4 v[8:9], v[40:43], off offset:96
	s_and_b64 exec, exec, s[44:45]
	s_cbranch_execz .LBB0_783
	v_cmp_gt_f32_e32 vcc, s80, v4
	s_mov_b32 s18, 0x3f317217
	v_lshl_add_u64 v[2:3], v[2:3], 2, s[12:13]
	v_cndmask_b32_e64 v5, 0, 32, vcc
	v_ldexp_f32 v4, v4, v5
	v_log_f32_e32 v4, v4
	v_cndmask_b32_e32 v5, 0, v226, vcc
	v_mul_f32_e32 v6, 0x3f317217, v4
	v_fma_f32 v6, v4, s18, -v6
	v_fmac_f32_e32 v6, 0x3377d1cf, v4
	s_mov_b32 s18, 0x7f800000
	v_fmac_f32_e32 v6, 0x3f317217, v4
	v_cmp_lt_f32_e64 vcc, |v4|, s18
	s_nop 1
	v_cndmask_b32_e32 v4, v4, v6, vcc
	v_sub_f32_e32 v4, v4, v5
	v_add_f32_e32 v0, v0, v4
	global_store_dword v[2:3], v0, off
	s_branch .LBB0_783
